# baseline (speedup 1.0000x reference)
.LBB6_8:
	v_cmp_lt_u32_e32 vcc, s15, v2
	s_and_saveexec_b64 s[10:11], vcc
	s_xor_b64 s[10:11], exec, s[10:11]
	s_cbranch_execz .LBB6_14
	v_cmp_lt_u32_e32 vcc, s3, v2
	s_and_saveexec_b64 s[12:13], vcc
	s_xor_b64 s[12:13], exec, s[12:13]
	s_cbranch_execz .LBB6_11
	v_and_b32_e32 v34, 0x7fffff80, v117
	v_lshl_add_u64 v[30:31], v[34:35], 2, v[36:37]
	v_add_co_u32_e32 v10, vcc, 0x4000, v30
	v_add_u32_e32 v67, 0x1020, v107
	s_nop 0
	v_addc_co_u32_e32 v11, vcc, 0, v31, vcc
	v_add_co_u32_e32 v18, vcc, 0x8000, v30
	global_load_dwordx4 v[2:5], v[30:31], off
	global_load_dwordx4 v[6:9], v[10:11], off
	v_addc_co_u32_e32 v19, vcc, 0, v31, vcc
	v_add_co_u32_e32 v20, vcc, 0xc000, v30
	v_add_u32_e32 v69, 0x1028, v107
	s_nop 0
	v_addc_co_u32_e32 v21, vcc, 0, v31, vcc
	v_add_co_u32_e32 v26, vcc, 0x10000, v30
	global_load_dwordx4 v[10:13], v[18:19], off
	global_load_dwordx4 v[14:17], v[20:21], off
	v_addc_co_u32_e32 v27, vcc, 0, v31, vcc
	v_add_co_u32_e32 v28, vcc, 0x14000, v30
	v_add_u32_e32 v71, 0x2040, v107
	s_nop 0
	v_addc_co_u32_e32 v29, vcc, 0, v31, vcc
	global_load_dwordx4 v[18:21], v[26:27], off
	global_load_dwordx4 v[22:25], v[28:29], off
	v_add_co_u32_e32 v26, vcc, 0x18000, v30
	v_add_u32_e32 v73, 0x2048, v107
	s_nop 0
	v_addc_co_u32_e32 v27, vcc, 0, v31, vcc
	global_load_dwordx4 v[26:29], v[26:27], off
	v_add_co_u32_e32 v30, vcc, 0x1c000, v30
	v_add_u32_e32 v75, 0x3060, v107
	s_nop 0
	v_addc_co_u32_e32 v31, vcc, 0, v31, vcc
	global_load_dwordx4 v[30:33], v[30:31], off
	v_add_u32_e32 v77, 0x3068, v107
	v_add_u32_e32 v79, 0x4080, v107
	v_add_u32_e32 v81, 0x4088, v107
	v_add_u32_e32 v83, 0x50a0, v107
	v_add_u32_e32 v85, 0x50a8, v107
	v_add_u32_e32 v87, 0x60c0, v107
	v_add_u32_e32 v89, 0x60c8, v107
	v_add_u32_e32 v91, 0x70e0, v107
	v_add_u32_e32 v93, 0x70e8, v107
	v_add_u32_e32 v95, 0x400, v111
	v_add_u32_e32 v97, 0x800, v111
	v_add_u32_e32 v99, 0xc00, v111
	v_add_u32_e32 v106, 0x1c00, v111
	v_add_u32_e32 v101, 0x1000, v111
	v_add_u32_e32 v102, 0x1400, v111
	v_add_u32_e32 v104, 0x1800, v111
	v_or_b32_e32 v34, v34, v109
	s_waitcnt vmcnt(7)
	ds_write2_b32 v107, v2, v3 offset1:1
	ds_write2_b32 v107, v4, v5 offset0:2 offset1:3
	s_waitcnt vmcnt(6)
	ds_write2_b32 v67, v6, v7 offset1:1
	ds_write2_b32 v69, v8, v9 offset1:1
	s_waitcnt vmcnt(5)
	ds_write2_b32 v71, v10, v11 offset1:1
	ds_write2_b32 v73, v12, v13 offset1:1
	s_waitcnt vmcnt(4)
	ds_write2_b32 v75, v14, v15 offset1:1
	ds_write2_b32 v77, v16, v17 offset1:1
	s_waitcnt vmcnt(3)
	ds_write2_b32 v79, v18, v19 offset1:1
	ds_write2_b32 v81, v20, v21 offset1:1
	s_waitcnt vmcnt(2)
	ds_write2_b32 v83, v22, v23 offset1:1
	ds_write2_b32 v85, v24, v25 offset1:1
	s_waitcnt vmcnt(1)
	ds_write2_b32 v87, v26, v27 offset1:1
	ds_write2_b32 v89, v28, v29 offset1:1
	s_waitcnt vmcnt(0)
	ds_write2_b32 v91, v30, v31 offset1:1
	ds_write2_b32 v93, v32, v33 offset1:1
	s_waitcnt lgkmcnt(0)
	s_barrier
	ds_read2_b32 v[6:7], v111 offset1:129
	ds_read2_b32 v[2:3], v99 offset0:6 offset1:135
	ds_read2_b32 v[8:9], v97 offset0:4 offset1:133
	ds_read2_b32 v[10:11], v95 offset0:2 offset1:131
	v_mad_u64_u32 v[12:13], s[20:21], v34, s16, v[38:39]
	s_waitcnt lgkmcnt(2)
	v_cvt_pk_f16_f32 v5, v2, v3
	s_waitcnt lgkmcnt(1)
	v_cvt_pk_f16_f32 v4, v8, v9
	s_waitcnt lgkmcnt(0)
	v_cvt_pk_f16_f32 v3, v10, v11
	v_cvt_pk_f16_f32 v2, v6, v7
	ds_read2_b32 v[6:7], v106 offset0:14 offset1:143
	ds_read2_b32 v[8:9], v104 offset0:12 offset1:141
	ds_read2_b32 v[10:11], v102 offset0:10 offset1:139
	ds_read2_b32 v[14:15], v101 offset0:8 offset1:137
	global_store_dwordx4 v[12:13], v[2:5], off
	s_waitcnt lgkmcnt(3)
	s_nop 0
	v_cvt_pk_f16_f32 v5, v6, v7
	s_waitcnt lgkmcnt(2)
	v_cvt_pk_f16_f32 v4, v8, v9
	s_waitcnt lgkmcnt(1)
	v_cvt_pk_f16_f32 v3, v10, v11
	s_waitcnt lgkmcnt(0)
	v_cvt_pk_f16_f32 v2, v14, v15
	v_add_u32_e32 v14, 0x2000, v111
	v_add_u32_e32 v10, 0x2400, v111
	v_add_u32_e32 v8, 0x2800, v111
	v_add_u32_e32 v6, 0x2c00, v111
	ds_read2_b32 v[6:7], v6 offset0:22 offset1:151
	ds_read2_b32 v[8:9], v8 offset0:20 offset1:149
	ds_read2_b32 v[10:11], v10 offset0:18 offset1:147
	ds_read2_b32 v[14:15], v14 offset0:16 offset1:145
	global_store_dwordx4 v[12:13], v[2:5], off offset:16
	s_waitcnt lgkmcnt(3)
	s_nop 0
	v_cvt_pk_f16_f32 v5, v6, v7
	s_waitcnt lgkmcnt(2)
	v_cvt_pk_f16_f32 v4, v8, v9
	s_waitcnt lgkmcnt(1)
	v_cvt_pk_f16_f32 v3, v10, v11
	s_waitcnt lgkmcnt(0)
	v_cvt_pk_f16_f32 v2, v14, v15
	v_add_u32_e32 v14, 0x3000, v111
	v_add_u32_e32 v10, 0x3400, v111
	v_add_u32_e32 v8, 0x3800, v111
	v_add_u32_e32 v6, 0x3c00, v111
	ds_read2_b32 v[6:7], v6 offset0:30 offset1:159
	ds_read2_b32 v[8:9], v8 offset0:28 offset1:157
	ds_read2_b32 v[10:11], v10 offset0:26 offset1:155
	ds_read2_b32 v[14:15], v14 offset0:24 offset1:153
	global_store_dwordx4 v[12:13], v[2:5], off offset:32
	s_waitcnt lgkmcnt(3)
	s_nop 0
	v_cvt_pk_f16_f32 v5, v6, v7
	s_waitcnt lgkmcnt(2)
	v_cvt_pk_f16_f32 v4, v8, v9
	s_waitcnt lgkmcnt(1)
	v_cvt_pk_f16_f32 v3, v10, v11
	s_waitcnt lgkmcnt(0)
	v_cvt_pk_f16_f32 v2, v14, v15
	global_store_dwordx4 v[12:13], v[2:5], off offset:48
	s_barrier
.LBB6_11:
	s_andn2_saveexec_b64 s[12:13], s[12:13]
	s_cbranch_execz .LBB6_13
	v_and_b32_e32 v34, 0x7fffff80, v119
	v_lshl_add_u64 v[30:31], v[34:35], 2, v[40:41]
	v_add_co_u32_e32 v10, vcc, 0x4000, v30
	v_add_u32_e32 v67, 0x1020, v107
	s_nop 0
	v_addc_co_u32_e32 v11, vcc, 0, v31, vcc
	v_add_co_u32_e32 v18, vcc, 0x8000, v30
	global_load_dwordx4 v[2:5], v[30:31], off
	global_load_dwordx4 v[6:9], v[10:11], off
	v_addc_co_u32_e32 v19, vcc, 0, v31, vcc
	v_add_co_u32_e32 v20, vcc, 0xc000, v30
	v_add_u32_e32 v69, 0x1028, v107
	s_nop 0
	v_addc_co_u32_e32 v21, vcc, 0, v31, vcc
	v_add_co_u32_e32 v26, vcc, 0x10000, v30
	global_load_dwordx4 v[10:13], v[18:19], off
	global_load_dwordx4 v[14:17], v[20:21], off
	v_addc_co_u32_e32 v27, vcc, 0, v31, vcc
	v_add_co_u32_e32 v28, vcc, 0x14000, v30
	v_add_u32_e32 v71, 0x2040, v107
	s_nop 0
	v_addc_co_u32_e32 v29, vcc, 0, v31, vcc
	global_load_dwordx4 v[18:21], v[26:27], off
	global_load_dwordx4 v[22:25], v[28:29], off
	v_add_co_u32_e32 v26, vcc, 0x18000, v30
	v_add_u32_e32 v73, 0x2048, v107
	s_nop 0
	v_addc_co_u32_e32 v27, vcc, 0, v31, vcc
	global_load_dwordx4 v[26:29], v[26:27], off
	v_add_co_u32_e32 v30, vcc, 0x1c000, v30
	v_add_u32_e32 v75, 0x3060, v107
	s_nop 0
	v_addc_co_u32_e32 v31, vcc, 0, v31, vcc
	global_load_dwordx4 v[30:33], v[30:31], off
	v_add_u32_e32 v77, 0x3068, v107
	v_add_u32_e32 v79, 0x4080, v107
	v_add_u32_e32 v81, 0x4088, v107
	v_add_u32_e32 v83, 0x50a0, v107
	v_add_u32_e32 v85, 0x50a8, v107
	v_add_u32_e32 v87, 0x60c0, v107
	v_add_u32_e32 v89, 0x60c8, v107
	v_add_u32_e32 v91, 0x70e0, v107
	v_add_u32_e32 v93, 0x70e8, v107
	v_add_u32_e32 v95, 0x400, v111
	v_add_u32_e32 v97, 0x800, v111
	v_add_u32_e32 v99, 0xc00, v111
	v_add_u32_e32 v106, 0x1c00, v111
	v_add_u32_e32 v101, 0x1000, v111
	v_add_u32_e32 v102, 0x1400, v111
	v_add_u32_e32 v104, 0x1800, v111
	v_or_b32_e32 v34, v34, v109
	s_waitcnt vmcnt(7)
	ds_write2_b32 v107, v2, v3 offset1:1
	ds_write2_b32 v107, v4, v5 offset0:2 offset1:3
	s_waitcnt vmcnt(6)
	ds_write2_b32 v67, v6, v7 offset1:1
	ds_write2_b32 v69, v8, v9 offset1:1
	s_waitcnt vmcnt(5)
	ds_write2_b32 v71, v10, v11 offset1:1
	ds_write2_b32 v73, v12, v13 offset1:1
	s_waitcnt vmcnt(4)
	ds_write2_b32 v75, v14, v15 offset1:1
	ds_write2_b32 v77, v16, v17 offset1:1
	s_waitcnt vmcnt(3)
	ds_write2_b32 v79, v18, v19 offset1:1
	ds_write2_b32 v81, v20, v21 offset1:1
	s_waitcnt vmcnt(2)
	ds_write2_b32 v83, v22, v23 offset1:1
	ds_write2_b32 v85, v24, v25 offset1:1
	s_waitcnt vmcnt(1)
	ds_write2_b32 v87, v26, v27 offset1:1
	ds_write2_b32 v89, v28, v29 offset1:1
	s_waitcnt vmcnt(0)
	ds_write2_b32 v91, v30, v31 offset1:1
	ds_write2_b32 v93, v32, v33 offset1:1
	s_waitcnt lgkmcnt(0)
	s_barrier
	ds_read2_b32 v[6:7], v111 offset1:129
	ds_read2_b32 v[2:3], v99 offset0:6 offset1:135
	ds_read2_b32 v[8:9], v97 offset0:4 offset1:133
	ds_read2_b32 v[10:11], v95 offset0:2 offset1:131
	v_mad_u64_u32 v[12:13], s[20:21], v34, s17, v[42:43]
	s_waitcnt lgkmcnt(2)
	v_cvt_pk_f16_f32 v5, v2, v3
	s_waitcnt lgkmcnt(1)
	v_cvt_pk_f16_f32 v4, v8, v9
	s_waitcnt lgkmcnt(0)
	v_cvt_pk_f16_f32 v3, v10, v11
	v_cvt_pk_f16_f32 v2, v6, v7
	ds_read2_b32 v[6:7], v106 offset0:14 offset1:143
	ds_read2_b32 v[8:9], v104 offset0:12 offset1:141
	ds_read2_b32 v[10:11], v102 offset0:10 offset1:139
	ds_read2_b32 v[14:15], v101 offset0:8 offset1:137
	global_store_dwordx4 v[12:13], v[2:5], off
	s_waitcnt lgkmcnt(3)
	s_nop 0
	v_cvt_pk_f16_f32 v5, v6, v7
	s_waitcnt lgkmcnt(2)
	v_cvt_pk_f16_f32 v4, v8, v9
	s_waitcnt lgkmcnt(1)
	v_cvt_pk_f16_f32 v3, v10, v11
	s_waitcnt lgkmcnt(0)
	v_cvt_pk_f16_f32 v2, v14, v15
	v_add_u32_e32 v14, 0x2000, v111
	v_add_u32_e32 v10, 0x2400, v111
	v_add_u32_e32 v8, 0x2800, v111
	v_add_u32_e32 v6, 0x2c00, v111
	ds_read2_b32 v[6:7], v6 offset0:22 offset1:151
	ds_read2_b32 v[8:9], v8 offset0:20 offset1:149
	ds_read2_b32 v[10:11], v10 offset0:18 offset1:147
	ds_read2_b32 v[14:15], v14 offset0:16 offset1:145
	global_store_dwordx4 v[12:13], v[2:5], off offset:16
	s_waitcnt lgkmcnt(3)
	s_nop 0
	v_cvt_pk_f16_f32 v5, v6, v7
	s_waitcnt lgkmcnt(2)
	v_cvt_pk_f16_f32 v4, v8, v9
	s_waitcnt lgkmcnt(1)
	v_cvt_pk_f16_f32 v3, v10, v11
	s_waitcnt lgkmcnt(0)
	v_cvt_pk_f16_f32 v2, v14, v15
	v_add_u32_e32 v14, 0x3000, v111
	v_add_u32_e32 v10, 0x3400, v111
	v_add_u32_e32 v8, 0x3800, v111
	v_add_u32_e32 v6, 0x3c00, v111
	ds_read2_b32 v[6:7], v6 offset0:30 offset1:159
	ds_read2_b32 v[8:9], v8 offset0:28 offset1:157
	ds_read2_b32 v[10:11], v10 offset0:26 offset1:155
	ds_read2_b32 v[14:15], v14 offset0:24 offset1:153
	global_store_dwordx4 v[12:13], v[2:5], off offset:32
	s_waitcnt lgkmcnt(3)
	s_nop 0
	v_cvt_pk_f16_f32 v5, v6, v7
	s_waitcnt lgkmcnt(2)
	v_cvt_pk_f16_f32 v4, v8, v9
	s_waitcnt lgkmcnt(1)
	v_cvt_pk_f16_f32 v3, v10, v11
	s_waitcnt lgkmcnt(0)
	v_cvt_pk_f16_f32 v2, v14, v15
	global_store_dwordx4 v[12:13], v[2:5], off offset:48
	s_barrier

.LBB6_14:
	s_andn2_saveexec_b64 s[10:11], s[10:11]
	s_cbranch_execz .LBB6_18
	v_add_u32_e32 v2, 0x800, v119
	v_and_b32_e32 v34, 0x7fffff80, v2
	v_lshl_add_u64 v[30:31], v[34:35], 2, v[44:45]
	v_mov_b32_e32 v67, v35
	v_lshl_add_u64 v[2:3], v[30:31], 0, v[66:67]
	global_load_dwordx4 v[2:5], v[2:3], off
	v_mov_b32_e32 v69, v35
	v_lshl_add_u64 v[6:7], v[30:31], 0, v[68:69]
	global_load_dwordx4 v[6:9], v[6:7], off
	v_mov_b32_e32 v71, v35
	v_lshl_add_u64 v[10:11], v[30:31], 0, v[70:71]
	global_load_dwordx4 v[10:13], v[10:11], off
	v_mov_b32_e32 v73, v35
	v_mov_b32_e32 v75, v35
	v_mov_b32_e32 v77, v35
	v_mov_b32_e32 v79, v35
	v_mov_b32_e32 v81, v35
	v_lshl_add_u64 v[14:15], v[30:31], 0, v[72:73]
	v_lshl_add_u64 v[18:19], v[30:31], 0, v[74:75]
	v_lshl_add_u64 v[22:23], v[30:31], 0, v[76:77]
	v_lshl_add_u64 v[26:27], v[30:31], 0, v[78:79]
	v_lshl_add_u64 v[128:129], v[30:31], 0, v[80:81]
	global_load_dwordx4 v[14:17], v[14:15], off
	s_nop 0
	global_load_dwordx4 v[18:21], v[18:19], off
	s_nop 0
	global_load_dwordx4 v[22:25], v[22:23], off
	s_nop 0
	global_load_dwordx4 v[26:29], v[26:27], off
	s_nop 0
	global_load_dwordx4 v[30:33], v[128:129], off
	global_load_dword v130, v[50:51], off
	global_load_dword v102, v[52:53], off
	global_load_dword v132, v[50:51], off offset:32
	global_load_dword v104, v[52:53], off offset:32
	global_load_dword v134, v[50:51], off offset:64
	global_load_dword v106, v[52:53], off offset:64
	global_load_dword v126, v[50:51], off offset:96
	global_load_dword v108, v[52:53], off offset:96
	global_load_dword v124, v[50:51], off offset:128
	global_load_dword v110, v[52:53], off offset:128
	global_load_dword v122, v[50:51], off offset:160
	global_load_dword v112, v[52:53], off offset:160
	global_load_dword v120, v[50:51], off offset:192
	global_load_dword v114, v[52:53], off offset:192
	global_load_dword v118, v[50:51], off offset:224
	global_load_dword v116, v[52:53], off offset:224
	s_waitcnt vmcnt(15)
	v_pk_mul_f32 v[128:129], v[2:3], v[130:131] op_sel_hi:[1,0]
	s_nop 0
	v_cvt_pk_f16_f32 v67, v128, v129
	v_cvt_f32_f16_e32 v128, v67
	v_cvt_f32_f16_sdwa v129, v67 dst_sel:DWORD dst_unused:UNUSED_PAD src0_sel:WORD_1
	s_waitcnt vmcnt(14)
	v_pk_fma_f32 v[2:3], v[2:3], v[102:103], 0 op_sel_hi:[1,0,0]
	v_pk_add_f32 v[136:137], v[128:129], 0 op_sel_hi:[1,0]
	ds_write2_b32 v107, v128, v129 offset1:1
	s_waitcnt vmcnt(13)
	v_pk_mul_f32 v[128:129], v[6:7], v[132:133] op_sel_hi:[1,0]
	s_waitcnt vmcnt(12)
	v_pk_fma_f32 v[2:3], v[6:7], v[104:105], v[2:3] op_sel_hi:[1,0,1]
	v_cvt_pk_f16_f32 v67, v128, v129
	v_cvt_f32_f16_e32 v128, v67
	v_cvt_f32_f16_sdwa v129, v67 dst_sel:DWORD dst_unused:UNUSED_PAD src0_sel:WORD_1
	v_add_u32_e32 v67, 0x1020, v107
	s_waitcnt vmcnt(10)
	v_pk_fma_f32 v[2:3], v[10:11], v[106:107], v[2:3] op_sel_hi:[1,0,1]
	v_pk_add_f32 v[136:137], v[136:137], v[128:129]
	ds_write2_b32 v67, v128, v129 offset1:1
	v_pk_mul_f32 v[128:129], v[10:11], v[134:135] op_sel_hi:[1,0]
	s_waitcnt vmcnt(8)
	v_pk_fma_f32 v[2:3], v[14:15], v[108:109], v[2:3] op_sel_hi:[1,0,1]
	v_cvt_pk_f16_f32 v67, v128, v129
	v_cvt_f32_f16_e32 v128, v67
	v_cvt_f32_f16_sdwa v129, v67 dst_sel:DWORD dst_unused:UNUSED_PAD src0_sel:WORD_1
	v_add_u32_e32 v67, 0x2040, v107
	s_waitcnt vmcnt(6)
	v_pk_fma_f32 v[2:3], v[18:19], v[110:111], v[2:3] op_sel_hi:[1,0,1]
	v_add_u32_e32 v10, 0x1028, v107
	v_pk_add_f32 v[136:137], v[136:137], v[128:129]
	ds_write2_b32 v67, v128, v129 offset1:1
	v_pk_mul_f32 v[128:129], v[14:15], v[126:127] op_sel_hi:[1,0]
	s_waitcnt vmcnt(4)
	v_pk_fma_f32 v[2:3], v[22:23], v[112:113], v[2:3] op_sel_hi:[1,0,1]
	v_cvt_pk_f16_f32 v67, v128, v129
	v_cvt_f32_f16_e32 v128, v67
	v_cvt_f32_f16_sdwa v129, v67 dst_sel:DWORD dst_unused:UNUSED_PAD src0_sel:WORD_1
	v_add_u32_e32 v67, 0x3060, v107
	s_waitcnt vmcnt(2)
	v_pk_fma_f32 v[2:3], v[26:27], v[114:115], v[2:3] op_sel_hi:[1,0,1]
	v_pk_add_f32 v[136:137], v[136:137], v[128:129]
	ds_write2_b32 v67, v128, v129 offset1:1
	v_pk_mul_f32 v[128:129], v[18:19], v[124:125] op_sel_hi:[1,0]
	s_waitcnt vmcnt(0)
	v_pk_fma_f32 v[2:3], v[30:31], v[116:117], v[2:3] op_sel_hi:[1,0,1]
	v_cvt_pk_f16_f32 v67, v128, v129
	v_cvt_f32_f16_e32 v128, v67
	v_cvt_f32_f16_sdwa v129, v67 dst_sel:DWORD dst_unused:UNUSED_PAD src0_sel:WORD_1
	v_add_u32_e32 v67, 0x4080, v107
	v_pk_add_f32 v[136:137], v[136:137], v[128:129]
	ds_write2_b32 v67, v128, v129 offset1:1
	v_pk_mul_f32 v[128:129], v[22:23], v[122:123] op_sel_hi:[1,0]
	s_nop 0
	v_cvt_pk_f16_f32 v67, v128, v129
	v_cvt_f32_f16_e32 v128, v67
	v_cvt_f32_f16_sdwa v129, v67 dst_sel:DWORD dst_unused:UNUSED_PAD src0_sel:WORD_1
	v_add_u32_e32 v67, 0x50a0, v107
	v_pk_add_f32 v[136:137], v[136:137], v[128:129]
	ds_write2_b32 v67, v128, v129 offset1:1
	v_pk_mul_f32 v[128:129], v[26:27], v[120:121] op_sel_hi:[1,0]
	s_nop 0
	v_cvt_pk_f16_f32 v67, v128, v129
	v_cvt_f32_f16_e32 v128, v67
	v_cvt_f32_f16_sdwa v129, v67 dst_sel:DWORD dst_unused:UNUSED_PAD src0_sel:WORD_1
	v_add_u32_e32 v67, 0x60c0, v107
	v_pk_add_f32 v[136:137], v[136:137], v[128:129]
	ds_write2_b32 v67, v128, v129 offset1:1
	v_pk_mul_f32 v[128:129], v[30:31], v[118:119] op_sel_hi:[1,0]
	s_nop 0
	v_cvt_pk_f16_f32 v67, v128, v129
	v_cvt_f32_f16_e32 v128, v67
	v_cvt_f32_f16_sdwa v129, v67 dst_sel:DWORD dst_unused:UNUSED_PAD src0_sel:WORD_1
	v_add_u32_e32 v67, 0x70e0, v107
	v_pk_add_f32 v[136:137], v[136:137], v[128:129]
	ds_write2_b32 v67, v128, v129 offset1:1
	ds_write_b64 v113, v[136:137] offset:33088
	ds_write_b64 v113, v[2:3] offset:37184
	v_pk_mul_f32 v[2:3], v[4:5], v[130:131] op_sel_hi:[1,0]
	s_nop 0
	v_cvt_pk_f16_f32 v3, v2, v3
	v_cvt_f32_f16_e32 v2, v3
	v_cvt_f32_f16_sdwa v3, v3 dst_sel:DWORD dst_unused:UNUSED_PAD src0_sel:WORD_1
	v_pk_add_f32 v[6:7], v[2:3], 0 op_sel_hi:[1,0]
	ds_write2_b32 v107, v2, v3 offset0:2 offset1:3
	v_pk_mul_f32 v[2:3], v[8:9], v[132:133] op_sel_hi:[1,0]
	s_nop 0
	v_cvt_pk_f16_f32 v3, v2, v3
	v_cvt_f32_f16_e32 v2, v3
	v_cvt_f32_f16_sdwa v3, v3 dst_sel:DWORD dst_unused:UNUSED_PAD src0_sel:WORD_1
	v_pk_add_f32 v[6:7], v[6:7], v[2:3]
	ds_write2_b32 v10, v2, v3 offset1:1
	v_pk_mul_f32 v[2:3], v[12:13], v[134:135] op_sel_hi:[1,0]
	v_add_u32_e32 v10, 0x2048, v107
	v_cvt_pk_f16_f32 v3, v2, v3
	v_cvt_f32_f16_e32 v2, v3
	v_cvt_f32_f16_sdwa v3, v3 dst_sel:DWORD dst_unused:UNUSED_PAD src0_sel:WORD_1
	v_pk_add_f32 v[6:7], v[6:7], v[2:3]
	ds_write2_b32 v10, v2, v3 offset1:1
	v_pk_mul_f32 v[2:3], v[16:17], v[126:127] op_sel_hi:[1,0]
	v_add_u32_e32 v10, 0x3068, v107
	v_cvt_pk_f16_f32 v3, v2, v3
	v_cvt_f32_f16_e32 v2, v3
	v_cvt_f32_f16_sdwa v3, v3 dst_sel:DWORD dst_unused:UNUSED_PAD src0_sel:WORD_1
	v_pk_add_f32 v[6:7], v[6:7], v[2:3]
	ds_write2_b32 v10, v2, v3 offset1:1
	v_pk_mul_f32 v[2:3], v[20:21], v[124:125] op_sel_hi:[1,0]
	v_add_u32_e32 v10, 0x4088, v107
	v_cvt_pk_f16_f32 v3, v2, v3
	v_cvt_f32_f16_e32 v2, v3
	v_cvt_f32_f16_sdwa v3, v3 dst_sel:DWORD dst_unused:UNUSED_PAD src0_sel:WORD_1
	v_pk_add_f32 v[6:7], v[6:7], v[2:3]
	ds_write2_b32 v10, v2, v3 offset1:1
	v_pk_mul_f32 v[2:3], v[24:25], v[122:123] op_sel_hi:[1,0]
	v_add_u32_e32 v10, 0x50a8, v107
	v_cvt_pk_f16_f32 v3, v2, v3
	v_cvt_f32_f16_e32 v2, v3
	v_cvt_f32_f16_sdwa v3, v3 dst_sel:DWORD dst_unused:UNUSED_PAD src0_sel:WORD_1
	v_pk_add_f32 v[6:7], v[6:7], v[2:3]
	ds_write2_b32 v10, v2, v3 offset1:1
	v_pk_mul_f32 v[2:3], v[28:29], v[120:121] op_sel_hi:[1,0]
	v_add_u32_e32 v10, 0x60c8, v107
	v_cvt_pk_f16_f32 v3, v2, v3
	v_cvt_f32_f16_e32 v2, v3
	v_cvt_f32_f16_sdwa v3, v3 dst_sel:DWORD dst_unused:UNUSED_PAD src0_sel:WORD_1
	v_pk_add_f32 v[6:7], v[6:7], v[2:3]
	ds_write2_b32 v10, v2, v3 offset1:1
	v_pk_mul_f32 v[2:3], v[32:33], v[118:119] op_sel_hi:[1,0]
	v_add_u32_e32 v10, 0x70e8, v107
	v_cvt_pk_f16_f32 v3, v2, v3
	v_cvt_f32_f16_e32 v2, v3
	v_cvt_f32_f16_sdwa v3, v3 dst_sel:DWORD dst_unused:UNUSED_PAD src0_sel:WORD_1
	v_pk_add_f32 v[6:7], v[6:7], v[2:3]
	ds_write2_b32 v10, v2, v3 offset1:1
	ds_write_b64 v113, v[6:7] offset:33096
	v_pk_fma_f32 v[2:3], v[4:5], v[102:103], 0 op_sel_hi:[1,0,0]
	v_add_u32_e32 v4, 0x800, v111
	v_pk_fma_f32 v[2:3], v[8:9], v[104:105], v[2:3] op_sel_hi:[1,0,1]
	s_nop 0
	v_pk_fma_f32 v[2:3], v[12:13], v[106:107], v[2:3] op_sel_hi:[1,0,1]
	s_nop 0
	v_pk_fma_f32 v[2:3], v[16:17], v[108:109], v[2:3] op_sel_hi:[1,0,1]
	s_nop 0
	v_pk_fma_f32 v[2:3], v[20:21], v[110:111], v[2:3] op_sel_hi:[1,0,1]
	s_nop 0
	v_pk_fma_f32 v[2:3], v[24:25], v[112:113], v[2:3] op_sel_hi:[1,0,1]
	s_nop 0
	v_pk_fma_f32 v[2:3], v[28:29], v[114:115], v[2:3] op_sel_hi:[1,0,1]
	s_nop 0
	v_pk_fma_f32 v[2:3], v[32:33], v[116:117], v[2:3] op_sel_hi:[1,0,1]
	ds_write_b64 v113, v[2:3] offset:37192
	v_or_b32_e32 v2, v34, v109
	s_waitcnt lgkmcnt(0)
	s_barrier
	v_mad_u64_u32 v[6:7], s[12:13], v2, s17, v[46:47]
	v_add_u32_e32 v2, 0x400, v111
	ds_read2_b32 v[10:11], v4 offset0:4 offset1:133
	v_add_u32_e32 v4, 0xc00, v111
	ds_read2_b32 v[8:9], v111 offset1:129
	ds_read2_b32 v[2:3], v2 offset0:2 offset1:131
	ds_read2_b32 v[4:5], v4 offset0:6 offset1:135
	s_waitcnt lgkmcnt(1)
	v_cvt_pk_f16_f32 v3, v2, v3
	s_waitcnt lgkmcnt(0)
	v_cvt_pk_f16_f32 v5, v4, v5
	v_cvt_pk_f16_f32 v4, v10, v11
	v_cvt_pk_f16_f32 v2, v8, v9
	global_store_dwordx4 v[6:7], v[2:5], off
	s_nop 1
	v_add_u32_e32 v2, 0x1000, v111
	v_add_u32_e32 v4, 0x1800, v111
	ds_read2_b32 v[8:9], v2 offset0:8 offset1:137
	v_add_u32_e32 v2, 0x1400, v111
	ds_read2_b32 v[10:11], v4 offset0:12 offset1:141
	v_add_u32_e32 v4, 0x1c00, v111
	ds_read2_b32 v[2:3], v2 offset0:10 offset1:139
	ds_read2_b32 v[4:5], v4 offset0:14 offset1:143
	s_waitcnt lgkmcnt(1)
	v_cvt_pk_f16_f32 v3, v2, v3
	s_waitcnt lgkmcnt(0)
	v_cvt_pk_f16_f32 v5, v4, v5
	v_cvt_pk_f16_f32 v4, v10, v11
	v_cvt_pk_f16_f32 v2, v8, v9
	global_store_dwordx4 v[6:7], v[2:5], off offset:16
	s_nop 1
	v_add_u32_e32 v2, 0x2000, v111
	v_add_u32_e32 v4, 0x2800, v111
	ds_read2_b32 v[8:9], v2 offset0:16 offset1:145
	v_add_u32_e32 v2, 0x2400, v111
	ds_read2_b32 v[10:11], v4 offset0:20 offset1:149
	v_add_u32_e32 v4, 0x2c00, v111
	ds_read2_b32 v[2:3], v2 offset0:18 offset1:147
	ds_read2_b32 v[4:5], v4 offset0:22 offset1:151
	s_waitcnt lgkmcnt(1)
	v_cvt_pk_f16_f32 v3, v2, v3
	s_waitcnt lgkmcnt(0)
	v_cvt_pk_f16_f32 v5, v4, v5
	v_cvt_pk_f16_f32 v4, v10, v11
	v_cvt_pk_f16_f32 v2, v8, v9
	global_store_dwordx4 v[6:7], v[2:5], off offset:32
	s_nop 1
	v_add_u32_e32 v2, 0x3000, v111
	v_add_u32_e32 v4, 0x3800, v111
	ds_read2_b32 v[8:9], v2 offset0:24 offset1:153
	v_add_u32_e32 v2, 0x3400, v111
	ds_read2_b32 v[10:11], v4 offset0:28 offset1:157
	v_add_u32_e32 v4, 0x3c00, v111
	ds_read2_b32 v[2:3], v2 offset0:26 offset1:155
	ds_read2_b32 v[4:5], v4 offset0:30 offset1:159
	s_waitcnt lgkmcnt(1)
	v_cvt_pk_f16_f32 v3, v2, v3
	s_waitcnt lgkmcnt(0)
	v_cvt_pk_f16_f32 v5, v4, v5
	v_cvt_pk_f16_f32 v4, v10, v11
	v_cvt_pk_f16_f32 v2, v8, v9
	global_store_dwordx4 v[6:7], v[2:5], off offset:48
	s_and_saveexec_b64 s[12:13], s[4:5]
	s_cbranch_execz .LBB6_17
	v_add_u32_e32 v10, 64, v115
	ds_read2st64_b32 v[2:3], v10 offset0:129 offset1:131
	ds_read2st64_b32 v[4:5], v10 offset0:145 offset1:147
	ds_read2st64_b32 v[6:7], v10 offset0:133 offset1:135
	ds_read2st64_b32 v[8:9], v10 offset0:149 offset1:151
	s_waitcnt lgkmcnt(3)
	v_add_f32_e32 v2, 0, v2
	s_waitcnt lgkmcnt(2)
	v_add_f32_e32 v4, 0, v4
	v_add_f32_e32 v2, v2, v3
	v_add_f32_e32 v4, v4, v5
	s_waitcnt lgkmcnt(1)
	v_add_f32_e32 v5, v2, v6
	ds_read2st64_b32 v[2:3], v10 offset0:137 offset1:139
	s_waitcnt lgkmcnt(1)
	v_add_f32_e32 v6, v4, v8
	v_add_f32_e32 v7, v5, v7
	ds_read2st64_b32 v[4:5], v10 offset0:153 offset1:155
	v_add_f32_e32 v11, v6, v9
	s_waitcnt lgkmcnt(1)
	v_add_f32_e32 v2, v7, v2
	ds_read2st64_b32 v[6:7], v10 offset0:141 offset1:143
	ds_read2st64_b32 v[8:9], v10 offset0:157 offset1:159
	v_add_f32_e32 v2, v2, v3
	s_waitcnt lgkmcnt(2)
	v_add_f32_e32 v4, v11, v4
	v_add_f32_e32 v3, v4, v5
	s_waitcnt lgkmcnt(1)
	v_add_f32_e32 v2, v2, v6
	s_waitcnt lgkmcnt(0)
	v_add_f32_e32 v3, v3, v8
	v_add_f32_e32 v6, v2, v7
	v_add_f32_e32 v7, v3, v9
	v_lshlrev_b64 v[2:3], 2, v[34:35]
	v_lshl_add_u64 v[4:5], v[54:55], 0, v[2:3]
	v_lshl_add_u64 v[2:3], v[56:57], 0, v[2:3]
	global_store_dword v[4:5], v6, off
	global_store_dword v[2:3], v7, off

.LBB6_19:
	s_and_b64 vcc, exec, s[6:7]
	s_mov_b64 s[12:13], s[10:11]
	s_cbranch_vccz .LBB6_23
	v_ashrrev_i32_e32 v11, 5, v2
	v_mov_b32_e32 v3, s34
	v_mov_b32_e32 v4, s30
	v_cmp_eq_u32_e32 vcc, 1, v11
	v_mov_b32_e32 v5, s31
	v_mov_b32_e32 v83, v35
	v_cndmask_b32_e32 v4, v3, v4, vcc
	v_mov_b32_e32 v3, s35
	v_cndmask_b32_e32 v3, v3, v5, vcc
	v_mov_b32_e32 v5, s29
	v_cmp_gt_u32_e32 vcc, 32, v2
	v_mov_b32_e32 v2, s28
	v_mov_b32_e32 v85, v35
	v_cndmask_b32_e32 v3, v3, v5, vcc
	v_cndmask_b32_e32 v2, v4, v2, vcc
	v_lshl_add_u64 v[2:3], v[2:3], 0, v[82:83]
	v_lshl_add_u64 v[12:13], v[2:3], 0, v[84:85]
	v_mov_b32_e32 v87, v35
	v_lshl_add_u64 v[22:23], v[12:13], 0, v[86:87]
	v_mov_b32_e32 v89, v35
	global_load_dword v20, v[58:59], off
	global_load_dword v14, v[58:59], off offset:32
	global_load_dword v16, v[58:59], off offset:64
	global_load_dword v18, v[58:59], off offset:96
	global_load_dword v10, v[58:59], off offset:128
	v_lshl_add_u64 v[24:25], v[12:13], 0, v[88:89]
	global_load_dwordx4 v[6:9], v[22:23], off
	global_load_dwordx4 v[2:5], v[24:25], off
	global_load_dword v34, v[60:61], off
	v_mov_b32_e32 v91, v35
	v_mov_b32_e32 v93, v35
	v_lshl_add_u64 v[30:31], v[12:13], 0, v[90:91]
	v_mov_b32_e32 v95, v35
	v_lshl_add_u64 v[32:33], v[12:13], 0, v[92:93]
	global_load_dwordx4 v[22:25], v[30:31], off
	global_load_dwordx4 v[26:29], v[32:33], off
	v_lshl_add_u64 v[120:121], v[12:13], 0, v[94:95]
	global_load_dwordx4 v[30:33], v[120:121], off
	global_load_dword v102, v[60:61], off offset:32
	global_load_dword v104, v[60:61], off offset:64
	global_load_dword v106, v[60:61], off offset:96
	global_load_dword v108, v[58:59], off offset:160
	v_mov_b32_e32 v97, v35
	v_lshl_add_u64 v[120:121], v[12:13], 0, v[96:97]
	global_load_dwordx4 v[120:123], v[120:121], off
	v_mov_b32_e32 v99, v35
	v_lshl_add_u64 v[128:129], v[12:13], 0, v[98:99]
	global_load_dwordx4 v[124:127], v[128:129], off
	global_load_dword v110, v[58:59], off offset:192
	global_load_dword v112, v[58:59], off offset:224
	v_mov_b32_e32 v101, v35
	v_lshl_add_u64 v[12:13], v[12:13], 0, v[100:101]
	global_load_dwordx4 v[128:131], v[12:13], off
	global_load_dword v114, v[60:61], off offset:128
	global_load_dword v116, v[60:61], off offset:160
	global_load_dword v118, v[60:61], off offset:192
	global_load_dword v132, v[60:61], off offset:224
	v_add_u32_e32 v67, 0x1020, v107
	v_add_u32_e32 v69, 0x2040, v107
	v_add_u32_e32 v71, 0x3060, v107
	s_waitcnt vmcnt(18)
	v_pk_mul_f32 v[12:13], v[6:7], v[20:21] op_sel_hi:[1,0]
	v_pk_mul_f32 v[20:21], v[8:9], v[20:21] op_sel_hi:[1,0]
	s_waitcnt vmcnt(16)
	v_pk_fma_f32 v[6:7], v[6:7], v[34:35], 0 op_sel_hi:[1,0,0]
	v_pk_fma_f32 v[8:9], v[8:9], v[34:35], 0 op_sel_hi:[1,0,0]
	v_pk_mul_f32 v[134:135], v[2:3], v[14:15] op_sel_hi:[1,0]
	v_pk_mul_f32 v[14:15], v[4:5], v[14:15] op_sel_hi:[1,0]
	s_waitcnt vmcnt(13)
	v_pk_mul_f32 v[140:141], v[30:31], v[10:11] op_sel_hi:[1,0]
	s_waitcnt vmcnt(12)
	v_pk_fma_f32 v[2:3], v[2:3], v[102:103], v[6:7] op_sel_hi:[1,0,1]
	v_pk_fma_f32 v[4:5], v[4:5], v[102:103], v[8:9] op_sel_hi:[1,0,1]
	v_cvt_pk_f16_f32 v9, v12, v13
	v_cvt_pk_f16_f32 v7, v134, v135
	v_pk_mul_f32 v[136:137], v[22:23], v[16:17] op_sel_hi:[1,0]
	v_cvt_f32_f16_e32 v6, v7
	v_cvt_f32_f16_sdwa v7, v7 dst_sel:DWORD dst_unused:UNUSED_PAD src0_sel:WORD_1
	v_cvt_f32_f16_e32 v8, v9
	v_cvt_f32_f16_sdwa v9, v9 dst_sel:DWORD dst_unused:UNUSED_PAD src0_sel:WORD_1
	v_pk_mul_f32 v[138:139], v[26:27], v[18:19] op_sel_hi:[1,0]
	v_cvt_pk_f16_f32 v13, v136, v137
	v_cvt_pk_f16_f32 v34, v138, v139
	v_cvt_f32_f16_e32 v12, v13
	v_cvt_f32_f16_sdwa v13, v13 dst_sel:DWORD dst_unused:UNUSED_PAD src0_sel:WORD_1
	s_waitcnt vmcnt(11)
	v_pk_fma_f32 v[2:3], v[22:23], v[104:105], v[2:3] op_sel_hi:[1,0,1]
	v_cvt_f32_f16_e32 v22, v34
	v_cvt_f32_f16_sdwa v23, v34 dst_sel:DWORD dst_unused:UNUSED_PAD src0_sel:WORD_1
	ds_write2_b32 v67, v6, v7 offset1:1
	ds_write2_b32 v107, v8, v9 offset1:1
	v_pk_add_f32 v[8:9], v[8:9], 0 op_sel_hi:[1,0]
	ds_write2_b32 v69, v12, v13 offset1:1
	ds_write2_b32 v71, v22, v23 offset1:1
	v_pk_add_f32 v[6:7], v[8:9], v[6:7]
	v_cvt_pk_f16_f32 v9, v140, v141
	v_pk_add_f32 v[6:7], v[6:7], v[12:13]
	s_waitcnt vmcnt(8)
	v_pk_mul_f32 v[12:13], v[120:121], v[108:109] op_sel_hi:[1,0]
	v_cvt_f32_f16_e32 v8, v9
	v_cvt_f32_f16_sdwa v9, v9 dst_sel:DWORD dst_unused:UNUSED_PAD src0_sel:WORD_1
	v_cvt_pk_f16_f32 v13, v12, v13
	v_cvt_f32_f16_e32 v12, v13
	v_cvt_f32_f16_sdwa v13, v13 dst_sel:DWORD dst_unused:UNUSED_PAD src0_sel:WORD_1
	v_pk_add_f32 v[6:7], v[6:7], v[22:23]
	v_add_u32_e32 v22, 0x4080, v107
	ds_write2_b32 v22, v8, v9 offset1:1
	v_pk_add_f32 v[6:7], v[6:7], v[8:9]
	v_add_u32_e32 v8, 0x50a0, v107
	ds_write2_b32 v8, v12, v13 offset1:1
	s_waitcnt vmcnt(6)
	v_pk_mul_f32 v[8:9], v[124:125], v[110:111] op_sel_hi:[1,0]
	v_pk_add_f32 v[6:7], v[6:7], v[12:13]
	v_cvt_pk_f16_f32 v9, v8, v9
	s_waitcnt vmcnt(4)
	v_pk_mul_f32 v[12:13], v[128:129], v[112:113] op_sel_hi:[1,0]
	v_cvt_f32_f16_e32 v8, v9
	v_cvt_f32_f16_sdwa v9, v9 dst_sel:DWORD dst_unused:UNUSED_PAD src0_sel:WORD_1
	v_cvt_pk_f16_f32 v13, v12, v13
	v_cvt_f32_f16_e32 v12, v13
	v_cvt_f32_f16_sdwa v13, v13 dst_sel:DWORD dst_unused:UNUSED_PAD src0_sel:WORD_1
	v_add_u32_e32 v22, 0x60c0, v107
	v_pk_add_f32 v[6:7], v[6:7], v[8:9]
	v_pk_fma_f32 v[2:3], v[26:27], v[106:107], v[2:3] op_sel_hi:[1,0,1]
	ds_write2_b32 v22, v8, v9 offset1:1
	v_add_u32_e32 v8, 0x70e0, v107
	v_pk_add_f32 v[6:7], v[6:7], v[12:13]
	ds_write2_b32 v8, v12, v13 offset1:1
	ds_write_b64 v113, v[6:7] offset:33088
	s_waitcnt vmcnt(3)
	v_pk_fma_f32 v[2:3], v[30:31], v[114:115], v[2:3] op_sel_hi:[1,0,1]
	v_cvt_pk_f16_f32 v9, v20, v21
	v_cvt_pk_f16_f32 v7, v14, v15
	s_waitcnt vmcnt(2)
	v_pk_fma_f32 v[2:3], v[120:121], v[116:117], v[2:3] op_sel_hi:[1,0,1]
	v_cvt_f32_f16_e32 v6, v7
	v_cvt_f32_f16_sdwa v7, v7 dst_sel:DWORD dst_unused:UNUSED_PAD src0_sel:WORD_1
	v_cvt_f32_f16_e32 v8, v9
	v_cvt_f32_f16_sdwa v9, v9 dst_sel:DWORD dst_unused:UNUSED_PAD src0_sel:WORD_1
	s_waitcnt vmcnt(1)
	v_pk_fma_f32 v[2:3], v[124:125], v[118:119], v[2:3] op_sel_hi:[1,0,1]
	v_pk_mul_f32 v[16:17], v[24:25], v[16:17] op_sel_hi:[1,0]
	s_waitcnt vmcnt(0)
	v_pk_fma_f32 v[2:3], v[128:129], v[132:133], v[2:3] op_sel_hi:[1,0,1]
	ds_write_b64 v113, v[2:3] offset:37184
	v_add_u32_e32 v2, 0x1028, v107
	ds_write2_b32 v2, v6, v7 offset1:1
	ds_write2_b32 v107, v8, v9 offset0:2 offset1:3
	v_pk_add_f32 v[2:3], v[8:9], 0 op_sel_hi:[1,0]
	v_pk_mul_f32 v[18:19], v[28:29], v[18:19] op_sel_hi:[1,0]
	v_pk_add_f32 v[2:3], v[2:3], v[6:7]
	v_cvt_pk_f16_f32 v7, v16, v17
	v_cvt_f32_f16_e32 v6, v7
	v_cvt_f32_f16_sdwa v7, v7 dst_sel:DWORD dst_unused:UNUSED_PAD src0_sel:WORD_1
	v_cvt_pk_f16_f32 v9, v18, v19
	v_cvt_f32_f16_e32 v8, v9
	v_cvt_f32_f16_sdwa v9, v9 dst_sel:DWORD dst_unused:UNUSED_PAD src0_sel:WORD_1
	v_add_u32_e32 v12, 0x2048, v107
	ds_write2_b32 v12, v6, v7 offset1:1
	v_pk_add_f32 v[2:3], v[2:3], v[6:7]
	v_add_u32_e32 v6, 0x3068, v107
	ds_write2_b32 v6, v8, v9 offset1:1
	v_pk_mul_f32 v[6:7], v[32:33], v[10:11] op_sel_hi:[1,0]
	v_pk_add_f32 v[2:3], v[2:3], v[8:9]
	v_cvt_pk_f16_f32 v7, v6, v7
	v_pk_mul_f32 v[8:9], v[122:123], v[108:109] op_sel_hi:[1,0]
	v_cvt_f32_f16_e32 v6, v7
	v_cvt_f32_f16_sdwa v7, v7 dst_sel:DWORD dst_unused:UNUSED_PAD src0_sel:WORD_1
	v_cvt_pk_f16_f32 v9, v8, v9
	v_cvt_f32_f16_e32 v8, v9
	v_cvt_f32_f16_sdwa v9, v9 dst_sel:DWORD dst_unused:UNUSED_PAD src0_sel:WORD_1
	v_add_u32_e32 v10, 0x4088, v107
	ds_write2_b32 v10, v6, v7 offset1:1
	v_pk_add_f32 v[2:3], v[2:3], v[6:7]
	v_add_u32_e32 v6, 0x50a8, v107
	ds_write2_b32 v6, v8, v9 offset1:1
	v_pk_mul_f32 v[6:7], v[126:127], v[110:111] op_sel_hi:[1,0]
	v_pk_add_f32 v[2:3], v[2:3], v[8:9]
	v_cvt_pk_f16_f32 v7, v6, v7
	v_pk_mul_f32 v[8:9], v[130:131], v[112:113] op_sel_hi:[1,0]
	v_cvt_f32_f16_e32 v6, v7
	v_cvt_f32_f16_sdwa v7, v7 dst_sel:DWORD dst_unused:UNUSED_PAD src0_sel:WORD_1
	v_cvt_pk_f16_f32 v9, v8, v9
	v_cvt_f32_f16_e32 v8, v9
	v_cvt_f32_f16_sdwa v9, v9 dst_sel:DWORD dst_unused:UNUSED_PAD src0_sel:WORD_1
	v_pk_fma_f32 v[4:5], v[24:25], v[104:105], v[4:5] op_sel_hi:[1,0,1]
	v_add_u32_e32 v10, 0x60c8, v107
	v_pk_add_f32 v[2:3], v[2:3], v[6:7]
	v_pk_fma_f32 v[4:5], v[28:29], v[106:107], v[4:5] op_sel_hi:[1,0,1]
	ds_write2_b32 v10, v6, v7 offset1:1
	v_add_u32_e32 v6, 0x70e8, v107
	v_pk_add_f32 v[2:3], v[2:3], v[8:9]
	ds_write2_b32 v6, v8, v9 offset1:1
	ds_write_b64 v113, v[2:3] offset:33096
	v_pk_fma_f32 v[2:3], v[32:33], v[114:115], v[4:5] op_sel_hi:[1,0,1]
	v_add_u32_e32 v4, 0x400, v111
	v_pk_fma_f32 v[2:3], v[122:123], v[116:117], v[2:3] op_sel_hi:[1,0,1]
	v_add_u32_e32 v5, 0x800, v111
	v_pk_fma_f32 v[2:3], v[126:127], v[118:119], v[2:3] op_sel_hi:[1,0,1]
	v_add_u32_e32 v10, 0x1000, v111
	v_pk_fma_f32 v[2:3], v[130:131], v[132:133], v[2:3] op_sel_hi:[1,0,1]
	ds_write_b64 v113, v[2:3] offset:37192
	v_add_u32_e32 v2, 0xc00, v111
	s_waitcnt lgkmcnt(0)
	s_barrier
	ds_read2_b32 v[6:7], v111 offset1:129
	ds_read2_b32 v[2:3], v2 offset0:6 offset1:135
	ds_read2_b32 v[8:9], v5 offset0:4 offset1:133
	ds_read2_b32 v[12:13], v4 offset0:2 offset1:131
	v_mad_i64_i32 v[14:15], s[12:13], v11, s18, v[48:49]
	s_waitcnt lgkmcnt(2)
	v_cvt_pk_f16_f32 v5, v2, v3
	s_waitcnt lgkmcnt(1)
	v_cvt_pk_f16_f32 v4, v8, v9
	s_waitcnt lgkmcnt(0)
	v_cvt_pk_f16_f32 v3, v12, v13
	v_cvt_pk_f16_f32 v2, v6, v7
	v_add_u32_e32 v12, 0x1400, v111
	v_add_u32_e32 v8, 0x1800, v111
	v_add_u32_e32 v6, 0x1c00, v111
	ds_read2_b32 v[6:7], v6 offset0:14 offset1:143
	ds_read2_b32 v[8:9], v8 offset0:12 offset1:141
	ds_read2_b32 v[12:13], v12 offset0:10 offset1:139
	ds_read2_b32 v[16:17], v10 offset0:8 offset1:137
	global_store_dwordx4 v[14:15], v[2:5], off
	v_add_u32_e32 v10, 0x2000, v111
	s_waitcnt lgkmcnt(3)
	v_cvt_pk_f16_f32 v5, v6, v7
	s_waitcnt lgkmcnt(2)
	v_cvt_pk_f16_f32 v4, v8, v9
	s_waitcnt lgkmcnt(1)
	v_cvt_pk_f16_f32 v3, v12, v13
	v_add_u32_e32 v12, 0x2400, v111
	v_add_u32_e32 v8, 0x2800, v111
	v_add_u32_e32 v6, 0x2c00, v111
	s_waitcnt lgkmcnt(0)
	v_cvt_pk_f16_f32 v2, v16, v17
	ds_read2_b32 v[6:7], v6 offset0:22 offset1:151
	ds_read2_b32 v[8:9], v8 offset0:20 offset1:149
	ds_read2_b32 v[12:13], v12 offset0:18 offset1:147
	ds_read2_b32 v[16:17], v10 offset0:16 offset1:145
	global_store_dwordx4 v[14:15], v[2:5], off offset:16
	v_add_u32_e32 v10, 0x3000, v111
	s_waitcnt lgkmcnt(3)
	v_cvt_pk_f16_f32 v5, v6, v7
	s_waitcnt lgkmcnt(2)
	v_cvt_pk_f16_f32 v4, v8, v9
	s_waitcnt lgkmcnt(1)
	v_cvt_pk_f16_f32 v3, v12, v13
	v_add_u32_e32 v12, 0x3400, v111
	v_add_u32_e32 v8, 0x3800, v111
	v_add_u32_e32 v6, 0x3c00, v111
	s_waitcnt lgkmcnt(0)
	v_cvt_pk_f16_f32 v2, v16, v17
	ds_read2_b32 v[6:7], v6 offset0:30 offset1:159
	ds_read2_b32 v[8:9], v8 offset0:28 offset1:157
	ds_read2_b32 v[12:13], v12 offset0:26 offset1:155
	ds_read2_b32 v[16:17], v10 offset0:24 offset1:153
	global_store_dwordx4 v[14:15], v[2:5], off offset:32
	s_waitcnt lgkmcnt(3)
	s_nop 0
	v_cvt_pk_f16_f32 v5, v6, v7
	s_waitcnt lgkmcnt(2)
	v_cvt_pk_f16_f32 v4, v8, v9
	s_waitcnt lgkmcnt(1)
	v_cvt_pk_f16_f32 v3, v12, v13
	s_waitcnt lgkmcnt(0)
	v_cvt_pk_f16_f32 v2, v16, v17
	global_store_dwordx4 v[14:15], v[2:5], off offset:48
	s_and_saveexec_b64 s[12:13], s[4:5]
	s_cbranch_execz .LBB6_22
	v_add_u32_e32 v12, 64, v115
	ds_read2st64_b32 v[2:3], v12 offset0:129 offset1:131
	ds_read2st64_b32 v[4:5], v12 offset0:145 offset1:147
	ds_read2st64_b32 v[8:9], v12 offset0:133 offset1:135
	v_lshlrev_b32_e32 v6, 9, v11
	ds_read2st64_b32 v[10:11], v12 offset0:149 offset1:151
	s_waitcnt lgkmcnt(3)
	v_add_f32_e32 v2, 0, v2
	s_waitcnt lgkmcnt(2)
	v_add_f32_e32 v4, 0, v4
	v_add_f32_e32 v2, v2, v3
	v_add_f32_e32 v4, v4, v5
	s_waitcnt lgkmcnt(1)
	v_add_f32_e32 v5, v2, v8
	ds_read2st64_b32 v[2:3], v12 offset0:137 offset1:139
	s_waitcnt lgkmcnt(1)
	v_add_f32_e32 v8, v4, v10
	v_add_f32_e32 v9, v5, v9
	ds_read2st64_b32 v[4:5], v12 offset0:153 offset1:155
	v_add_f32_e32 v13, v8, v11
	s_waitcnt lgkmcnt(1)
	v_add_f32_e32 v2, v9, v2
	ds_read2st64_b32 v[8:9], v12 offset0:141 offset1:143
	ds_read2st64_b32 v[10:11], v12 offset0:157 offset1:159
	v_add_f32_e32 v2, v2, v3
	s_waitcnt lgkmcnt(2)
	v_add_f32_e32 v4, v13, v4
	v_add_f32_e32 v3, v4, v5
	v_ashrrev_i32_e32 v7, 31, v6
	s_waitcnt lgkmcnt(1)
	v_add_f32_e32 v2, v2, v8
	s_waitcnt lgkmcnt(0)
	v_add_f32_e32 v3, v3, v10
	v_add_f32_e32 v8, v2, v9
	v_add_f32_e32 v9, v3, v11
	v_lshlrev_b64 v[2:3], 2, v[6:7]
	v_lshl_add_u64 v[4:5], v[62:63], 0, v[2:3]
	v_lshl_add_u64 v[2:3], v[64:65], 0, v[2:3]
	global_store_dword v[4:5], v8, off
	global_store_dword v[2:3], v9, off
